# GDN chain compute: stores straight from packed regs, scalar 64-bit store address, no rotation moves
# baseline (speedup 1.0000x reference)
; #define LDS_BARRIER() asm volatile("s_waitcnt lgkmcnt(0)\n\ts_barrier" ::: "memory")
; __device__ void phase_gdn_chain(const Params& p, int l, char* smem, int vb, int nvb, int oz) {
;     ...
;             f32x4 S[4];
; #pragma unroll
;             for (int mt = 0; mt < 4; ++mt) S[mt] = (f32x4){0.f, 0.f, 0.f, 0.f};
;             bf16x4 ost[4], onew[4];
; #pragma unroll
;             for (int mt = 0; mt < 4; ++mt) { ost[mt] = (bf16x4){0, 0, 0, 0}; onew[mt] = (bf16x4){0, 0, 0, 0}; }
;             size_t orow = 0;
;             bool ohave = false;
;             if (__builtin_amdgcn_readfirstlane(wave) < 4) __builtin_amdgcn_s_setprio(3);
;             LDS_BARRIER();
.LBB0_393:
	s_ashr_i32 s47, s46, 31
	s_waitcnt lgkmcnt(0)
	s_barrier
	s_lshl_b32 s3, s2, 6
	s_lshl_b64 s[0:1], s[46:47], 8
	s_add_u32 s24, s0, 0x4000
	s_waitcnt vmcnt(0)
	v_mov_b32_e32 v84, 0
	v_mov_b32_e32 v68, 0
	s_addc_u32 s25, s1, 0
	s_lshl_b64 s[50:51], s[46:47], 11
	s_mov_b32 s26, 0
	s_mov_b64 s[54:55], 0
	s_mov_b64 s[52:53], 0
	v_mov_b32_e32 v162, 0
	v_mov_b32_e32 v163, 0
	v_mov_b32_e32 v156, 0
	v_mov_b32_e32 v157, 0
	v_mov_b32_e32 v158, 0
	v_mov_b32_e32 v159, 0
	v_mov_b32_e32 v160, 0
	v_mov_b32_e32 v161, 0
	v_mov_b32_e32 v69, v68
	v_mov_b32_e32 v70, v68
	v_mov_b32_e32 v71, v68
	v_mov_b32_e32 v72, v68
	v_mov_b32_e32 v73, v68
	v_mov_b32_e32 v74, v68
	v_mov_b32_e32 v75, v68
	v_mov_b32_e32 v76, v68
	v_mov_b32_e32 v77, v68
	v_mov_b32_e32 v78, v68
	v_mov_b32_e32 v79, v68
	v_mov_b32_e32 v80, v68
	v_mov_b32_e32 v81, v68
	v_mov_b32_e32 v82, v68
	v_mov_b32_e32 v83, v68
	v_mov_b32_e32 v85, v84
	v_mov_b32_e32 v86, v84
	v_mov_b32_e32 v87, v84
	v_mov_b32_e32 v88, v84
	v_mov_b32_e32 v89, v84
	v_mov_b32_e32 v90, v84
	v_mov_b32_e32 v91, v84
	v_mov_b32_e32 v185, 0
	v_mov_b64_e32 v[182:183], s[34:35]
	v_mad_u64_u32 v[182:183], s[4:5], v188, s92, v[182:183]
	v_mov_b32_e32 v184, v183
	v_mad_u64_u32 v[180:181], s[4:5], v189, s92, v[184:185]
	v_mov_b32_e32 v183, v180
	s_lshl_b32 s96, s81, 1
	v_lshl_add_u64 v[180:181], v[182:183], 0, s[96:97]
	s_lshl_b32 s96, s3, 1
	v_lshl_add_u64 v[180:181], v[180:181], 0, s[96:97]
	v_lshlrev_b32_e32 v184, 1, v194
	v_lshl_add_u64 v[180:181], v[180:181], 0, v[184:185]
	v_lshlrev_b32_e32 v184, 1, v192
	v_lshl_add_u64 v[186:187], v[180:181], 0, v[184:185]
	s_branch .LBB0_396

; #define LDS_BARRIER() asm volatile("s_waitcnt lgkmcnt(0)\n\ts_barrier" ::: "memory")
; __device__ void phase_gdn_chain(const Params& p, int l, char* smem, int vb, int nvb, int oz) {
;     ...
;             for (int ci = 0; ci < 36; ++ci) {
;                 if (ohave) {
; #pragma unroll
;                     for (int mt = 0; mt < 4; ++mt)
;                         *(bf16x4*)(U + (orow + 16 * mt + li) * LDU + C_GQ + dir * 256 + h * 64 + 16 * sl + 4 * g) = ost[mt];
;                 }
;     ...
;                 asm volatile("" :: "v"(ost[0]), "v"(ost[1]), "v"(ost[2]), "v"(ost[3]));
; #pragma unroll
;                 for (int mt = 0; mt < 4; ++mt) ost[mt] = onew[mt];
;                 LDS_BARRIER();
.LBB0_395:
	s_waitcnt lgkmcnt(0)
	s_barrier
	s_add_i32 s26, s26, 1
	s_cmp_eq_u32 s26, 36
	s_cbranch_scc1 .LBB0_417
.LBB0_396:
	s_cmp_gt_u32 s26, 3
	s_cselect_b64 s[56:57], -1, 0
	s_bitcmp1_b32 s26, 0
	s_cselect_b32 s0, 0xb210, 0
	s_add_i32 s0, s0, 0
	v_mov_b32_e32 v2, s0
	v_add3_u32 v84, s0, v203, v205
	ds_read2st64_b64 v[94:97], v84 offset0:72 offset1:76
	v_add3_u32 v172, s0, v191, v207
	ds_read_b32 v2, v2 offset:45568
	ds_read_b128 v[104:107], v172
	ds_read_b128 v[112:115], v172 offset:64
	ds_read_b128 v[124:127], v172 offset:2304
	ds_read2st64_b64 v[128:131], v84 offset0:80 offset1:84
	ds_read_b128 v[132:135], v172 offset:2368
	ds_read_b128 v[136:139], v172 offset:4608
	ds_read_b128 v[140:143], v172 offset:4672
	ds_read_b128 v[144:147], v172 offset:6912
	ds_read_b128 v[174:177], v172 offset:6976
	v_lshl_add_u32 v173, v192, 2, s0
	ds_read_b128 v[120:123], v173 offset:45312
	ds_read_b128 v[116:119], v173 offset:45376
	ds_read_b128 v[108:111], v173 offset:45440
	ds_read_b128 v[100:103], v173 offset:45504
	s_andn2_b64 vcc, exec, s[52:53]
	s_cbranch_vccnz .LBB0_398
	s_mul_i32 s6, s55, s92
	s_mul_hi_u32 s5, s54, s92
	s_mul_i32 s4, s54, s92
	s_add_u32 s5, s5, s6
	v_lshl_add_u64 v[180:181], s[4:5], 0, v[186:187]
	v_add_co_u32_e32 v182, vcc, 0x1a000, v180
	global_store_dwordx2 v[180:181], v[160:161], off offset:1024
	s_nop 0
	v_addc_co_u32_e32 v183, vcc, 0, v181, vcc
	global_store_dwordx2 v[182:183], v[158:159], off offset:3072
	v_add_co_u32_e32 v182, vcc, 0x35000, v180
	s_nop 1
	v_addc_co_u32_e32 v183, vcc, 0, v181, vcc
	v_add_co_u32_e32 v180, vcc, 0x4f000, v180
	global_store_dwordx2 v[182:183], v[156:157], off offset:1024
	s_nop 0
	v_addc_co_u32_e32 v181, vcc, 0, v181, vcc
	global_store_dwordx2 v[180:181], v[162:163], off offset:3072

; __device__ void phase_gdn_chain(const Params& p, int l, char* smem, int vb, int nvb, int oz) {
;     ...
;             if (ohave) {
; #pragma unroll
;                 for (int mt = 0; mt < 4; ++mt)
;                     *(bf16x4*)(U + (orow + 16 * mt + li) * LDU + C_GQ + dir * 256 + h * 64 + 16 * sl + 4 * g) = ost[mt];
;             }
.LBB0_417:
	v_lshl_add_u64 v[68:69], s[54:55], 0, v[188:189]
	v_mov_b64_e32 v[70:71], s[34:35]
	v_mad_u64_u32 v[70:71], s[0:1], v68, s92, v[70:71]
	v_mov_b32_e32 v2, v71
	v_mad_u64_u32 v[68:69], s[0:1], v69, s92, v[2:3]
	v_mov_b32_e32 v71, v68
	s_lshl_b32 s96, s81, 1
	v_lshl_add_u64 v[68:69], v[70:71], 0, s[96:97]
	s_lshl_b32 s96, s3, 1
	v_lshl_add_u64 v[68:69], v[68:69], 0, s[96:97]
	v_lshlrev_b32_e32 v2, 1, v194
	v_lshl_add_u64 v[68:69], v[68:69], 0, v[2:3]
	v_lshlrev_b32_e32 v2, 1, v192
	v_lshl_add_u64 v[68:69], v[68:69], 0, v[2:3]
	v_add_co_u32_e32 v70, vcc, 0x1a000, v68
	global_store_dwordx2 v[68:69], v[160:161], off offset:1024
	s_nop 0
	v_addc_co_u32_e32 v71, vcc, 0, v69, vcc
	global_store_dwordx2 v[70:71], v[158:159], off offset:3072
	v_add_co_u32_e32 v70, vcc, 0x35000, v68
	s_nop 1
	v_addc_co_u32_e32 v71, vcc, 0, v69, vcc
	v_add_co_u32_e32 v68, vcc, 0x4f000, v68
	global_store_dwordx2 v[70:71], v[156:157], off offset:1024
	s_nop 0
	v_addc_co_u32_e32 v69, vcc, 0, v69, vcc
	global_store_dwordx2 v[68:69], v[162:163], off offset:3072
